# COMB: all nine gathered rows of a token loaded up front (rows 3..8 into otherwise unused registers); ring reload sites became register copies
# speedup vs baseline: 1.0081x; 1.0081x over previous
.LBB0_916:
	s_or_b64 exec, exec, s[4:5]
	v_mov_b32_e32 v218, s35
	ds_read_b32 v219, v218
	ds_read_b32 v220, v218 offset:4
	ds_read_b32 v221, v218 offset:8
	ds_read_b32 v234, v218 offset:12
	ds_read_b32 v235, v218 offset:16
	ds_read_b32 v236, v218 offset:20
	s_waitcnt lgkmcnt(0)
	v_readfirstlane_b32 s4, v219
	s_ashr_i32 s5, s4, 31
	s_lshl_b64 s[4:5], s[4:5], 11
	v_lshl_add_u64 v[238:239], v[86:87], 0, s[4:5]
	global_load_dwordx2 v[166:167], v[238:239], off nt
	global_load_dwordx2 v[168:169], v[238:239], off offset:512 nt
	global_load_dwordx2 v[170:171], v[238:239], off offset:1024 nt
	global_load_dwordx2 v[172:173], v[238:239], off offset:1536 nt
	v_readfirstlane_b32 s4, v220
	s_ashr_i32 s5, s4, 31
	s_lshl_b64 s[4:5], s[4:5], 11
	v_lshl_add_u64 v[240:241], v[86:87], 0, s[4:5]
	global_load_dwordx2 v[174:175], v[240:241], off nt
	global_load_dwordx2 v[176:177], v[240:241], off offset:512 nt
	global_load_dwordx2 v[178:179], v[240:241], off offset:1024 nt
	global_load_dwordx2 v[180:181], v[240:241], off offset:1536 nt
	v_readfirstlane_b32 s4, v221
	s_ashr_i32 s5, s4, 31
	s_lshl_b64 s[4:5], s[4:5], 11
	v_lshl_add_u64 v[238:239], v[86:87], 0, s[4:5]
	global_load_dwordx2 v[182:183], v[238:239], off nt
	global_load_dwordx2 v[184:185], v[238:239], off offset:512 nt
	global_load_dwordx2 v[186:187], v[238:239], off offset:1024 nt
	global_load_dwordx2 v[188:189], v[238:239], off offset:1536 nt
	v_readfirstlane_b32 s4, v234
	s_ashr_i32 s5, s4, 31
	s_lshl_b64 s[4:5], s[4:5], 11
	v_lshl_add_u64 v[240:241], v[86:87], 0, s[4:5]
	global_load_dwordx2 v[190:191], v[240:241], off nt
	global_load_dwordx2 v[192:193], v[240:241], off offset:512 nt
	global_load_dwordx2 v[194:195], v[240:241], off offset:1024 nt
	global_load_dwordx2 v[196:197], v[240:241], off offset:1536 nt
	v_readfirstlane_b32 s4, v235
	s_ashr_i32 s5, s4, 31
	s_lshl_b64 s[4:5], s[4:5], 11
	v_lshl_add_u64 v[238:239], v[86:87], 0, s[4:5]
	global_load_dwordx2 v[202:203], v[238:239], off nt
	global_load_dwordx2 v[204:205], v[238:239], off offset:512 nt
	global_load_dwordx2 v[206:207], v[238:239], off offset:1024 nt
	global_load_dwordx2 v[208:209], v[238:239], off offset:1536 nt
	v_readfirstlane_b32 s4, v236
	s_ashr_i32 s5, s4, 31
	s_lshl_b64 s[4:5], s[4:5], 11
	v_lshl_add_u64 v[240:241], v[86:87], 0, s[4:5]
	global_load_dwordx2 v[210:211], v[240:241], off nt
	global_load_dwordx2 v[212:213], v[240:241], off offset:512 nt
	global_load_dwordx2 v[214:215], v[240:241], off offset:1024 nt
	global_load_dwordx2 v[216:217], v[240:241], off offset:1536 nt
	s_waitcnt vmcnt(38)
	v_lshlrev_b32_e32 v104, 16, v74
	v_and_b32_e32 v105, 0xffff0000, v74
	v_lshlrev_b32_e32 v74, 16, v75
	v_and_b32_e32 v75, 0xffff0000, v75
	v_pk_mul_f32 v[132:133], v[74:75], s[90:91] op_sel_hi:[1,0]
	v_lshlrev_b32_e32 v74, 16, v76
	v_and_b32_e32 v75, 0xffff0000, v76
	v_pk_mul_f32 v[130:131], v[74:75], s[90:91] op_sel_hi:[1,0]
	v_lshlrev_b32_e32 v74, 16, v77
	v_and_b32_e32 v75, 0xffff0000, v77
	v_pk_mul_f32 v[126:127], v[74:75], s[90:91] op_sel_hi:[1,0]
	s_waitcnt vmcnt(37)
	v_lshlrev_b32_e32 v74, 16, v70
	v_and_b32_e32 v75, 0xffff0000, v70
	v_lshlrev_b32_e32 v70, 16, v71
	v_and_b32_e32 v71, 0xffff0000, v71
	v_pk_mul_f32 v[124:125], v[70:71], s[90:91] op_sel_hi:[1,0]
	v_lshlrev_b32_e32 v70, 16, v72
	v_and_b32_e32 v71, 0xffff0000, v72
	v_pk_mul_f32 v[122:123], v[70:71], s[90:91] op_sel_hi:[1,0]
	v_lshlrev_b32_e32 v70, 16, v73
	v_and_b32_e32 v71, 0xffff0000, v73
	v_pk_mul_f32 v[118:119], v[70:71], s[90:91] op_sel_hi:[1,0]
	s_waitcnt vmcnt(36)
	v_lshlrev_b32_e32 v70, 16, v66
	v_and_b32_e32 v71, 0xffff0000, v66
	v_lshlrev_b32_e32 v66, 16, v67
	v_and_b32_e32 v67, 0xffff0000, v67
	v_pk_mul_f32 v[116:117], v[66:67], s[90:91] op_sel_hi:[1,0]
	v_lshlrev_b32_e32 v66, 16, v68
	v_and_b32_e32 v67, 0xffff0000, v68
	v_lshlrev_b32_e32 v96, 16, v78
	v_and_b32_e32 v97, 0xffff0000, v78
	v_lshlrev_b32_e32 v78, 16, v79
	v_and_b32_e32 v79, 0xffff0000, v79
	v_lshlrev_b32_e32 v98, 16, v80
	v_and_b32_e32 v99, 0xffff0000, v80
	v_lshlrev_b32_e32 v80, 16, v81
	v_and_b32_e32 v81, 0xffff0000, v81
	v_pk_mul_f32 v[114:115], v[66:67], s[90:91] op_sel_hi:[1,0]
	v_lshlrev_b32_e32 v66, 16, v69
	v_and_b32_e32 v67, 0xffff0000, v69
	v_pk_mul_f32 v[96:97], v[96:97], s[90:91] op_sel_hi:[1,0]
	v_pk_mul_f32 v[78:79], v[78:79], s[90:91] op_sel_hi:[1,0]
	v_pk_mul_f32 v[98:99], v[98:99], s[90:91] op_sel_hi:[1,0]
	v_pk_mul_f32 v[80:81], v[80:81], s[90:91] op_sel_hi:[1,0]
	v_pk_mul_f32 v[134:135], v[104:105], s[90:91] op_sel_hi:[1,0]
	v_pk_mul_f32 v[128:129], v[74:75], s[90:91] op_sel_hi:[1,0]
	v_pk_mul_f32 v[120:121], v[70:71], s[90:91] op_sel_hi:[1,0]
	v_pk_mul_f32 v[112:113], v[66:67], s[90:91] op_sel_hi:[1,0]
	s_mov_b32 s36, 0
	s_mov_b32 s37, s35
.LBB0_917:
	v_mov_b32_e32 v66, s37
	ds_read_b32 v66, v66 offset:52
	s_cmp_lt_u32 s36, 6
	s_cselect_b64 s[4:5], -1, 0
	s_cmp_gt_u32 s36, 5
	s_cselect_b64 s[26:27], -1, 0
	s_waitcnt lgkmcnt(0)
	v_readfirstlane_b32 s30, v66
	s_and_b64 vcc, exec, s[26:27]
	s_waitcnt vmcnt(35)
	v_mov_b32_e32 v66, v150
	v_mov_b32_e32 v67, v151
	s_waitcnt vmcnt(34)
	v_mov_b32_e32 v68, v148
	v_mov_b32_e32 v69, v149
	s_waitcnt vmcnt(33)
	v_mov_b32_e32 v70, v146
	v_mov_b32_e32 v71, v147
	s_waitcnt vmcnt(32)
	v_mov_b32_e32 v72, v144
	v_mov_b32_e32 v73, v145
	s_cbranch_vccnz .LBB0_919
.LBB0_919:
	v_mov_b32_e32 v74, s37
	ds_read_b32 v75, v74 offset:56
	v_cndmask_b32_e64 v76, 0, 1, s[4:5]
	s_waitcnt vmcnt(31)
	v_mov_b32_e32 v74, v110
	v_cmp_ne_u32_e64 s[10:11], 1, v76
	s_andn2_b64 vcc, exec, s[4:5]
	s_waitcnt lgkmcnt(0)
	v_readfirstlane_b32 s28, v75
	v_mov_b32_e32 v75, v111
	s_waitcnt vmcnt(30)
	v_mov_b32_e32 v76, v108
	v_mov_b32_e32 v77, v109
	s_waitcnt vmcnt(29)
	v_mov_b32_e32 v104, v102
	v_mov_b32_e32 v105, v103
	s_waitcnt vmcnt(28)
	v_mov_b32_e32 v106, v100
	v_mov_b32_e32 v107, v101
	s_cbranch_vccnz .LBB0_921
.LBB0_921:
	v_mov_b32_e32 v136, s37
	ds_read_b32 v138, v136 offset:60
	s_and_b64 vcc, exec, s[10:11]
	s_waitcnt vmcnt(24)
	v_mov_b64_e32 v[142:143], v[88:89]
	v_mov_b64_e32 v[140:141], v[90:91]
	v_mov_b64_e32 v[136:137], v[92:93]
	s_waitcnt lgkmcnt(0)
	v_readfirstlane_b32 s10, v138
	v_mov_b64_e32 v[138:139], v[94:95]
	s_cbranch_vccnz .LBB0_923
.LBB0_923:
	v_cvt_f32_fp8_e32 v164, v150
	v_cvt_f32_fp8_sdwa v165, v150 src0_sel:BYTE_1
	s_add_i32 s36, s36, 3
	s_add_i32 s37, s37, 12
	s_and_b64 vcc, exec, s[26:27]
	v_pk_fma_f32 v[96:97], v[164:165], s[30:31], v[96:97] op_sel_hi:[1,0,1]
	v_cvt_f32_fp8_sdwa v164, v150 src0_sel:BYTE_2
	v_cvt_f32_fp8_sdwa v165, v150 src0_sel:BYTE_3
	v_cvt_f32_fp8_sdwa v150, v151 src0_sel:BYTE_2
	v_pk_fma_f32 v[78:79], v[164:165], s[30:31], v[78:79] op_sel_hi:[1,0,1]
	v_cvt_f32_fp8_e32 v164, v151
	v_cvt_f32_fp8_sdwa v165, v151 src0_sel:BYTE_1
	v_cvt_f32_fp8_sdwa v151, v151 src0_sel:BYTE_3
	v_pk_fma_f32 v[98:99], v[164:165], s[30:31], v[98:99] op_sel_hi:[1,0,1]
	v_pk_fma_f32 v[80:81], v[150:151], s[30:31], v[80:81] op_sel_hi:[1,0,1]
	v_cvt_f32_fp8_e32 v150, v148
	v_cvt_f32_fp8_sdwa v151, v148 src0_sel:BYTE_1
	v_pk_fma_f32 v[134:135], v[150:151], s[30:31], v[134:135] op_sel_hi:[1,0,1]
	v_cvt_f32_fp8_sdwa v150, v148 src0_sel:BYTE_2
	v_cvt_f32_fp8_sdwa v151, v148 src0_sel:BYTE_3
	v_cvt_f32_fp8_sdwa v148, v149 src0_sel:BYTE_2
	v_pk_fma_f32 v[132:133], v[150:151], s[30:31], v[132:133] op_sel_hi:[1,0,1]
	v_cvt_f32_fp8_e32 v150, v149
	v_cvt_f32_fp8_sdwa v151, v149 src0_sel:BYTE_1
	v_cvt_f32_fp8_sdwa v149, v149 src0_sel:BYTE_3
	v_pk_fma_f32 v[130:131], v[150:151], s[30:31], v[130:131] op_sel_hi:[1,0,1]
	v_pk_fma_f32 v[126:127], v[148:149], s[30:31], v[126:127] op_sel_hi:[1,0,1]
	v_cvt_f32_fp8_e32 v148, v146
	v_cvt_f32_fp8_sdwa v149, v146 src0_sel:BYTE_1
	v_pk_fma_f32 v[128:129], v[148:149], s[30:31], v[128:129] op_sel_hi:[1,0,1]
	v_cvt_f32_fp8_sdwa v148, v146 src0_sel:BYTE_2
	v_cvt_f32_fp8_sdwa v149, v146 src0_sel:BYTE_3
	v_cvt_f32_fp8_sdwa v146, v147 src0_sel:BYTE_2
	v_pk_fma_f32 v[124:125], v[148:149], s[30:31], v[124:125] op_sel_hi:[1,0,1]
	v_cvt_f32_fp8_e32 v148, v147
	v_cvt_f32_fp8_sdwa v149, v147 src0_sel:BYTE_1
	v_cvt_f32_fp8_sdwa v147, v147 src0_sel:BYTE_3
	v_pk_fma_f32 v[122:123], v[148:149], s[30:31], v[122:123] op_sel_hi:[1,0,1]
	v_pk_fma_f32 v[118:119], v[146:147], s[30:31], v[118:119] op_sel_hi:[1,0,1]
	v_cvt_f32_fp8_e32 v146, v144
	v_cvt_f32_fp8_sdwa v147, v144 src0_sel:BYTE_1
	v_pk_fma_f32 v[120:121], v[146:147], s[30:31], v[120:121] op_sel_hi:[1,0,1]
	v_cvt_f32_fp8_sdwa v146, v144 src0_sel:BYTE_2
	v_cvt_f32_fp8_sdwa v147, v144 src0_sel:BYTE_3
	v_cvt_f32_fp8_sdwa v144, v145 src0_sel:BYTE_2
	v_pk_fma_f32 v[116:117], v[146:147], s[30:31], v[116:117] op_sel_hi:[1,0,1]
	v_cvt_f32_fp8_e32 v146, v145
	v_cvt_f32_fp8_sdwa v147, v145 src0_sel:BYTE_1
	v_cvt_f32_fp8_sdwa v145, v145 src0_sel:BYTE_3
	v_pk_fma_f32 v[114:115], v[146:147], s[30:31], v[114:115] op_sel_hi:[1,0,1]
	v_pk_fma_f32 v[112:113], v[144:145], s[30:31], v[112:113] op_sel_hi:[1,0,1]
	v_cvt_f32_fp8_e32 v144, v110
	v_cvt_f32_fp8_sdwa v145, v110 src0_sel:BYTE_1
	v_pk_fma_f32 v[96:97], v[144:145], s[28:29], v[96:97] op_sel_hi:[1,0,1]
	v_cvt_f32_fp8_sdwa v144, v110 src0_sel:BYTE_2
	v_cvt_f32_fp8_sdwa v145, v110 src0_sel:BYTE_3
	v_cvt_f32_fp8_sdwa v110, v111 src0_sel:BYTE_2
	v_pk_fma_f32 v[78:79], v[144:145], s[28:29], v[78:79] op_sel_hi:[1,0,1]
	v_cvt_f32_fp8_e32 v144, v111
	v_cvt_f32_fp8_sdwa v145, v111 src0_sel:BYTE_1
	v_cvt_f32_fp8_sdwa v111, v111 src0_sel:BYTE_3
	v_pk_fma_f32 v[98:99], v[144:145], s[28:29], v[98:99] op_sel_hi:[1,0,1]
	v_pk_fma_f32 v[80:81], v[110:111], s[28:29], v[80:81] op_sel_hi:[1,0,1]
	v_cvt_f32_fp8_e32 v110, v108
	v_cvt_f32_fp8_sdwa v111, v108 src0_sel:BYTE_1
	v_pk_fma_f32 v[110:111], v[110:111], s[28:29], v[134:135] op_sel_hi:[1,0,1]
	v_cvt_f32_fp8_sdwa v134, v108 src0_sel:BYTE_2
	v_cvt_f32_fp8_sdwa v135, v108 src0_sel:BYTE_3
	v_cvt_f32_fp8_sdwa v108, v109 src0_sel:BYTE_2
	v_pk_fma_f32 v[132:133], v[134:135], s[28:29], v[132:133] op_sel_hi:[1,0,1]
	v_cvt_f32_fp8_e32 v134, v109
	v_cvt_f32_fp8_sdwa v135, v109 src0_sel:BYTE_1
	v_cvt_f32_fp8_sdwa v109, v109 src0_sel:BYTE_3
	v_pk_fma_f32 v[130:131], v[134:135], s[28:29], v[130:131] op_sel_hi:[1,0,1]
	v_pk_fma_f32 v[108:109], v[108:109], s[28:29], v[126:127] op_sel_hi:[1,0,1]
	v_cvt_f32_fp8_e32 v126, v102
	v_cvt_f32_fp8_sdwa v127, v102 src0_sel:BYTE_1
	v_pk_fma_f32 v[128:129], v[126:127], s[28:29], v[128:129] op_sel_hi:[1,0,1]
	v_cvt_f32_fp8_sdwa v126, v102 src0_sel:BYTE_2
	v_cvt_f32_fp8_sdwa v127, v102 src0_sel:BYTE_3
	v_cvt_f32_fp8_sdwa v102, v103 src0_sel:BYTE_2
	v_pk_fma_f32 v[124:125], v[126:127], s[28:29], v[124:125] op_sel_hi:[1,0,1]
	v_cvt_f32_fp8_e32 v126, v103
	v_cvt_f32_fp8_sdwa v127, v103 src0_sel:BYTE_1
	v_cvt_f32_fp8_sdwa v103, v103 src0_sel:BYTE_3
	v_pk_fma_f32 v[122:123], v[126:127], s[28:29], v[122:123] op_sel_hi:[1,0,1]
	v_pk_fma_f32 v[102:103], v[102:103], s[28:29], v[118:119] op_sel_hi:[1,0,1]
	v_cvt_f32_fp8_e32 v118, v100
	v_cvt_f32_fp8_sdwa v119, v100 src0_sel:BYTE_1
	v_pk_fma_f32 v[120:121], v[118:119], s[28:29], v[120:121] op_sel_hi:[1,0,1]
	v_cvt_f32_fp8_sdwa v118, v100 src0_sel:BYTE_2
	v_cvt_f32_fp8_sdwa v119, v100 src0_sel:BYTE_3
	v_cvt_f32_fp8_sdwa v100, v101 src0_sel:BYTE_2
	v_pk_fma_f32 v[116:117], v[118:119], s[28:29], v[116:117] op_sel_hi:[1,0,1]
	v_cvt_f32_fp8_e32 v118, v101
	v_cvt_f32_fp8_sdwa v119, v101 src0_sel:BYTE_1
	v_cvt_f32_fp8_sdwa v101, v101 src0_sel:BYTE_3
	v_pk_fma_f32 v[114:115], v[118:119], s[28:29], v[114:115] op_sel_hi:[1,0,1]
	v_pk_fma_f32 v[100:101], v[100:101], s[28:29], v[112:113] op_sel_hi:[1,0,1]
	v_cvt_f32_fp8_e32 v112, v94
	v_cvt_f32_fp8_sdwa v113, v94 src0_sel:BYTE_1
	v_pk_fma_f32 v[96:97], v[112:113], s[10:11], v[96:97] op_sel_hi:[1,0,1]
	v_cvt_f32_fp8_sdwa v112, v94 src0_sel:BYTE_2
	v_cvt_f32_fp8_sdwa v113, v94 src0_sel:BYTE_3
	v_cvt_f32_fp8_sdwa v94, v95 src0_sel:BYTE_2
	v_pk_fma_f32 v[78:79], v[112:113], s[10:11], v[78:79] op_sel_hi:[1,0,1]
	v_cvt_f32_fp8_e32 v112, v95
	v_cvt_f32_fp8_sdwa v113, v95 src0_sel:BYTE_1
	v_cvt_f32_fp8_sdwa v95, v95 src0_sel:BYTE_3
	v_pk_fma_f32 v[98:99], v[112:113], s[10:11], v[98:99] op_sel_hi:[1,0,1]
	v_pk_fma_f32 v[80:81], v[94:95], s[10:11], v[80:81] op_sel_hi:[1,0,1]
	v_cvt_f32_fp8_e32 v94, v92
	v_cvt_f32_fp8_sdwa v95, v92 src0_sel:BYTE_1
	v_pk_fma_f32 v[134:135], v[94:95], s[10:11], v[110:111] op_sel_hi:[1,0,1]
	v_cvt_f32_fp8_sdwa v94, v92 src0_sel:BYTE_2
	v_cvt_f32_fp8_sdwa v95, v92 src0_sel:BYTE_3
	v_cvt_f32_fp8_sdwa v92, v93 src0_sel:BYTE_2
	v_pk_fma_f32 v[132:133], v[94:95], s[10:11], v[132:133] op_sel_hi:[1,0,1]
	v_cvt_f32_fp8_e32 v94, v93
	v_cvt_f32_fp8_sdwa v95, v93 src0_sel:BYTE_1
	v_cvt_f32_fp8_sdwa v93, v93 src0_sel:BYTE_3
	v_pk_fma_f32 v[130:131], v[94:95], s[10:11], v[130:131] op_sel_hi:[1,0,1]
	v_pk_fma_f32 v[126:127], v[92:93], s[10:11], v[108:109] op_sel_hi:[1,0,1]
	v_cvt_f32_fp8_e32 v92, v90
	v_cvt_f32_fp8_sdwa v93, v90 src0_sel:BYTE_1
	v_pk_fma_f32 v[128:129], v[92:93], s[10:11], v[128:129] op_sel_hi:[1,0,1]
	v_cvt_f32_fp8_sdwa v92, v90 src0_sel:BYTE_2
	v_cvt_f32_fp8_sdwa v93, v90 src0_sel:BYTE_3
	v_cvt_f32_fp8_sdwa v90, v91 src0_sel:BYTE_2
	v_pk_fma_f32 v[124:125], v[92:93], s[10:11], v[124:125] op_sel_hi:[1,0,1]
	v_cvt_f32_fp8_e32 v92, v91
	v_cvt_f32_fp8_sdwa v93, v91 src0_sel:BYTE_1
	v_cvt_f32_fp8_sdwa v91, v91 src0_sel:BYTE_3
	v_pk_fma_f32 v[122:123], v[92:93], s[10:11], v[122:123] op_sel_hi:[1,0,1]
	v_pk_fma_f32 v[118:119], v[90:91], s[10:11], v[102:103] op_sel_hi:[1,0,1]
	v_cvt_f32_fp8_e32 v90, v88
	v_cvt_f32_fp8_sdwa v91, v88 src0_sel:BYTE_1
	v_pk_fma_f32 v[120:121], v[90:91], s[10:11], v[120:121] op_sel_hi:[1,0,1]
	v_cvt_f32_fp8_sdwa v90, v88 src0_sel:BYTE_2
	v_cvt_f32_fp8_sdwa v91, v88 src0_sel:BYTE_3
	v_cvt_f32_fp8_sdwa v88, v89 src0_sel:BYTE_2
	v_pk_fma_f32 v[116:117], v[90:91], s[10:11], v[116:117] op_sel_hi:[1,0,1]
	v_cvt_f32_fp8_e32 v90, v89
	v_cvt_f32_fp8_sdwa v91, v89 src0_sel:BYTE_1
	v_cvt_f32_fp8_sdwa v89, v89 src0_sel:BYTE_3
	v_pk_fma_f32 v[114:115], v[90:91], s[10:11], v[114:115] op_sel_hi:[1,0,1]
	v_pk_fma_f32 v[112:113], v[88:89], s[10:11], v[100:101] op_sel_hi:[1,0,1]
	s_cbranch_vccnz .LBB0_925
	s_cmp_eq_u32 s36, 3
	s_cbranch_scc0 .Lcb_r6
	s_waitcnt vmcnt(12)
	v_mov_b64_e32 v[150:151], v[166:167]
	v_mov_b64_e32 v[148:149], v[168:169]
	v_mov_b64_e32 v[146:147], v[170:171]
	v_mov_b64_e32 v[144:145], v[172:173]
	v_mov_b64_e32 v[110:111], v[174:175]
	v_mov_b64_e32 v[108:109], v[176:177]
	v_mov_b64_e32 v[102:103], v[178:179]
	v_mov_b64_e32 v[100:101], v[180:181]
	v_mov_b64_e32 v[94:95], v[182:183]
	v_mov_b64_e32 v[92:93], v[184:185]
	v_mov_b64_e32 v[90:91], v[186:187]
	v_mov_b64_e32 v[88:89], v[188:189]
	s_branch .LBB0_917
.Lcb_r6:
	s_waitcnt vmcnt(0)
	v_mov_b64_e32 v[150:151], v[190:191]
	v_mov_b64_e32 v[148:149], v[192:193]
	v_mov_b64_e32 v[146:147], v[194:195]
	v_mov_b64_e32 v[144:145], v[196:197]
	v_mov_b64_e32 v[110:111], v[202:203]
	v_mov_b64_e32 v[108:109], v[204:205]
	v_mov_b64_e32 v[102:103], v[206:207]
	v_mov_b64_e32 v[100:101], v[208:209]
	v_mov_b64_e32 v[94:95], v[210:211]
	v_mov_b64_e32 v[92:93], v[212:213]
	v_mov_b64_e32 v[90:91], v[214:215]
	v_mov_b64_e32 v[88:89], v[216:217]
	s_branch .LBB0_917
